# v12
# speedup vs baseline: 1.0027x; 1.0027x over previous
.LBB0_3:
	s_cmpk_gt_u32 s2, 0x41
	s_cbranch_scc0 .LBB0_27
	s_load_dwordx2 s[4:5], s[0:1], 0x40
	s_load_dwordx2 s[6:7], s[0:1], 0x30
	s_cmpk_gt_u32 s2, 0x81
	s_mov_b64 s[12:13], -1
	s_cbranch_scc0 .LBB0_17
	s_load_dwordx2 s[20:21], s[0:1], 0x38
	s_load_dwordx2 s[22:23], s[0:1], 0x48
	s_load_dwordx2 s[24:25], s[0:1], 0x50
	s_movk_i32 s3, 0xc0
	v_cmp_gt_u32_e32 vcc, s3, v0
	s_and_saveexec_b64 s[12:13], vcc
	s_cbranch_execz .LBB0_7
	v_lshlrev_b32_e32 v2, 2, v0
	v_mov_b32_e32 v3, 0
	s_waitcnt lgkmcnt(0)
	v_lshl_add_u64 v[4:5], s[10:11], 0, v[2:3]
	v_add_co_u32_e32 v4, vcc, 0x1000, v4
	s_nop 1
	v_addc_co_u32_e32 v5, vcc, 0, v5, vcc
	global_store_dword v[4:5], v3, off offset:3328
.LBB0_7:
	s_or_b64 exec, exec, s[12:13]
	v_cmp_gt_u32_e32 vcc, 64, v0
	s_and_saveexec_b64 s[12:13], vcc
	s_cbranch_execz .LBB0_16
	s_load_dwordx2 s[14:15], s[0:1], 0x28
	v_mul_u32_u24_e32 v1, 12, v0
	v_lshl_or_b32 v2, v0, 2, 1
	v_lshlrev_b32_e32 v1, 2, v1
	v_mul_u32_u24_e32 v2, 3, v2
	v_lshlrev_b32_e32 v22, 2, v2
	s_waitcnt lgkmcnt(0)
	s_load_dword s26, s[20:21], 0x0
	s_load_dwordx2 s[28:29], s[22:23], 0x0
	s_load_dword s30, s[22:23], 0x8
	v_cmp_gt_u32_e32 vcc, 24, v0
	s_and_saveexec_b64 s[32:33], vcc
	v_lshrrev_b32_e32 v59, 1, v0
	v_lshlrev_b32_e32 v60, 1, v0
	v_lshl_or_b32 v59, v59, 2, 12
	v_and_b32_e32 v60, 48, v60
	v_mul_u32_u24_e32 v61, 3, v0
	v_lshlrev_b32_e32 v61, 2, v61
	global_load_dword v54, v59, s[24:25]
	global_load_dword v55, v60, s[24:25] offset:8
	global_load_dwordx3 v[56:58], v61, s[4:5]
	s_or_b64 exec, exec, s[32:33]
	global_load_dwordx3 v[18:20], v1, s[4:5] offset:288
	global_load_dwordx4 v[10:13], v22, s[4:5] offset:288
	global_load_dwordx4 v[14:17], v22, s[4:5] offset:304
	v_lshlrev_b32_e32 v1, 4, v0
	global_load_dwordx4 v[2:5], v1, s[14:15]
	global_load_dword v21, v22, s[4:5] offset:320
	global_load_dwordx4 v[6:9], v1, s[6:7]
	v_cmp_gt_u32_e32 vcc, 24, v0
	s_waitcnt vmcnt(5)
	v_mov_b32_e32 v22, v20
	s_waitcnt vmcnt(4)
	v_mov_b32_e32 v23, v12
	v_mov_b32_e32 v24, v13
	s_waitcnt vmcnt(2)
	v_pk_mul_f32 v[12:13], v[2:3], v[22:23]
	v_mov_b32_e32 v25, v14
	v_mov_b32_e32 v20, v15
	v_pk_fma_f32 v[14:15], v[2:3], v[18:19], 0 op_sel_hi:[0,1,0]
	v_add_f32_e32 v1, 0, v12
	s_waitcnt vmcnt(1)
	v_pk_mul_f32 v[18:19], v[4:5], v[20:21]
	v_pk_fma_f32 v[10:11], v[2:3], v[10:11], v[14:15] op_sel:[1,0,0]
	v_add_f32_e32 v1, v1, v13
	v_mov_b32_e32 v20, v5
	v_pk_fma_f32 v[10:11], v[4:5], v[24:25], v[10:11] op_sel_hi:[0,1,1]
	v_add_f32_e32 v1, v1, v18
	v_pk_fma_f32 v[10:11], v[20:21], v[16:17], v[10:11] op_sel_hi:[0,1,1]
	v_add_f32_e32 v1, v1, v19
	s_and_saveexec_b64 s[14:15], vcc
	s_cbranch_execz .LBB0_10
	v_bfe_u32 v17, v0, 1, 2
	v_mov_b32_e32 v18, -1.0
	v_cvt_f32_ubyte0_e32 v17, v17
	s_mov_b32 s3, 0xc2fc0000
	v_fmamk_f32 v17, v17, 0x3faaaaab, v18
	v_mov_b32_e32 v19, 0x42800000
	v_cmp_gt_f32_e32 vcc, s3, v17
	s_waitcnt vmcnt(1)
	v_sub_f32_e32 v15, v54, v55
	v_cndmask_b32_e32 v18, 0, v19, vcc
	v_add_f32_e32 v17, v17, v18
	v_exp_f32_e32 v17, v17
	v_not_b32_e32 v18, 63
	v_cndmask_b32_e32 v18, 0, v18, vcc
	v_ldexp_f32 v17, v17, v18
	v_mul_f32_e32 v15, v17, v15
	v_fract_f32_e32 v15, v15
	v_cos_f32_e32 v16, v15
	v_sin_f32_e32 v15, v15
	v_and_b32_e32 v17, 1, v0
	v_cmp_eq_u32_e32 vcc, 0, v17
	s_nop 1
	v_cndmask_b32_e32 v16, v16, v15, vcc
	s_waitcnt vmcnt(0)
	v_pk_fma_f32 v[10:11], v[56:57], v[16:17], v[10:11] op_sel_hi:[1,0,1]
	v_fmac_f32_e32 v1, v58, v16
.LBB0_10:
	s_or_b64 exec, exec, s[14:15]
	s_waitcnt vmcnt(0)
	v_fma_f32 v2, v2, v6, 0
	v_fmac_f32_e32 v2, v3, v7
	v_mbcnt_lo_u32_b32 v3, -1, 0
	v_mbcnt_hi_u32_b32 v3, -1, v3
	v_fmac_f32_e32 v2, v4, v8
	v_and_b32_e32 v4, 64, v3
	v_fmac_f32_e32 v2, v5, v9
	v_add_u32_e32 v5, 64, v4
	v_xor_b32_e32 v4, 32, v3
	v_cmp_lt_i32_e32 vcc, v4, v5
	s_mov_b64 s[14:15], s[22:23]
	s_nop 0
	v_cndmask_b32_e32 v4, v3, v4, vcc
	v_lshlrev_b32_e32 v4, 2, v4
	ds_bpermute_b32 v6, v4, v2
	ds_bpermute_b32 v7, v4, v10
	ds_bpermute_b32 v8, v4, v11
	ds_bpermute_b32 v4, v4, v1
	s_waitcnt lgkmcnt(0)
	v_add_f32_e32 v2, v2, v6
	v_add_f32_e32 v6, v10, v7
	v_add_f32_e32 v7, v11, v8
	v_add_f32_e32 v1, v1, v4
	v_xor_b32_e32 v4, 16, v3
	v_cmp_lt_i32_e32 vcc, v4, v5
	s_nop 1
	v_cndmask_b32_e32 v4, v3, v4, vcc
	v_lshlrev_b32_e32 v4, 2, v4
	ds_bpermute_b32 v8, v4, v2
	ds_bpermute_b32 v9, v4, v6
	ds_bpermute_b32 v10, v4, v7
	ds_bpermute_b32 v4, v4, v1
	s_waitcnt lgkmcnt(3)
	v_add_f32_e32 v2, v2, v8
	s_waitcnt lgkmcnt(2)
	v_add_f32_e32 v6, v6, v9
	s_waitcnt lgkmcnt(1)
	v_add_f32_e32 v7, v7, v10
	s_waitcnt lgkmcnt(0)
	v_add_f32_e32 v1, v1, v4
	v_xor_b32_e32 v4, 8, v3
	v_cmp_lt_i32_e32 vcc, v4, v5
	s_nop 1
	v_cndmask_b32_e32 v4, v3, v4, vcc
	v_lshlrev_b32_e32 v4, 2, v4
	ds_bpermute_b32 v8, v4, v2
	ds_bpermute_b32 v9, v4, v6
	ds_bpermute_b32 v10, v4, v7
	ds_bpermute_b32 v4, v4, v1
	s_waitcnt lgkmcnt(3)
	v_add_f32_e32 v2, v2, v8
	s_waitcnt lgkmcnt(2)
	v_add_f32_e32 v6, v6, v9
	s_waitcnt lgkmcnt(1)
	v_add_f32_e32 v7, v7, v10
	s_waitcnt lgkmcnt(0)
	v_add_f32_e32 v1, v1, v4
	v_xor_b32_e32 v4, 4, v3
	v_cmp_lt_i32_e32 vcc, v4, v5
	s_nop 1
	v_cndmask_b32_e32 v4, v3, v4, vcc
	v_lshlrev_b32_e32 v4, 2, v4
	ds_bpermute_b32 v8, v4, v2
	ds_bpermute_b32 v9, v4, v6
	ds_bpermute_b32 v10, v4, v7
	ds_bpermute_b32 v4, v4, v1
	s_waitcnt lgkmcnt(3)
	v_add_f32_e32 v2, v2, v8
	s_waitcnt lgkmcnt(2)
	v_add_f32_e32 v6, v6, v9
	s_waitcnt lgkmcnt(1)
	v_add_f32_e32 v7, v7, v10
	s_waitcnt lgkmcnt(0)
	v_add_f32_e32 v1, v1, v4
	v_xor_b32_e32 v4, 2, v3
	v_cmp_lt_i32_e32 vcc, v4, v5
	s_nop 1
	v_cndmask_b32_e32 v4, v3, v4, vcc
	v_lshlrev_b32_e32 v4, 2, v4
	ds_bpermute_b32 v8, v4, v2
	ds_bpermute_b32 v9, v4, v6
	ds_bpermute_b32 v10, v4, v7
	ds_bpermute_b32 v11, v4, v1
	s_waitcnt lgkmcnt(3)
	v_add_f32_e32 v8, v2, v8
	v_xor_b32_e32 v2, 1, v3
	v_cmp_lt_i32_e32 vcc, v2, v5
	s_waitcnt lgkmcnt(2)
	v_add_f32_e32 v6, v6, v9
	s_waitcnt lgkmcnt(1)
	v_add_f32_e32 v4, v7, v10
	v_cndmask_b32_e32 v2, v3, v2, vcc
	s_waitcnt lgkmcnt(0)
	v_add_f32_e32 v1, v1, v11
	v_lshlrev_b32_e32 v2, 2, v2
	ds_bpermute_b32 v9, v2, v8
	ds_bpermute_b32 v7, v2, v6
	ds_bpermute_b32 v5, v2, v4
	ds_bpermute_b32 v2, v2, v1
	v_mov_b32_e32 v3, 0
	v_cmp_eq_u32_e32 vcc, 0, v0
	s_and_saveexec_b64 s[16:17], vcc
	s_cbranch_execnz .LBB0_64
	s_or_b64 exec, exec, s[16:17]
	v_cmp_eq_u32_e32 vcc, 1, v0
	s_and_saveexec_b64 s[16:17], vcc
	s_cbranch_execnz .LBB0_65

.LBB0_14:
	s_mov_b32 s3, s30
	s_waitcnt lgkmcnt(0)
	v_add_f32_e32 v1, v1, v2
	v_add_f32_e32 v3, s3, v1

.LBB0_64:
	s_waitcnt lgkmcnt(0)
	v_add_f32_e32 v3, v8, v9
	s_mov_b32 s3, s26
	v_add_f32_e32 v3, s3, v3
	s_or_b64 exec, exec, s[16:17]
	v_cmp_eq_u32_e32 vcc, 1, v0
	s_and_saveexec_b64 s[16:17], vcc
	s_cbranch_execz .LBB0_12
.LBB0_65:
	s_mov_b32 s3, s28
	s_waitcnt lgkmcnt(0)
	v_add_f32_e32 v3, v6, v7
	v_add_f32_e32 v3, s3, v3
	s_or_b64 exec, exec, s[16:17]
	v_cmp_eq_u32_e32 vcc, 2, v0
	s_and_saveexec_b64 s[16:17], vcc
	s_cbranch_execz .LBB0_13
.LBB0_66:
	s_mov_b32 s3, s29
	s_waitcnt lgkmcnt(0)
	v_add_f32_e32 v3, v4, v5
	v_add_f32_e32 v3, s3, v3
	s_or_b64 exec, exec, s[16:17]
	v_cmp_eq_u32_e32 vcc, 3, v0
	s_and_saveexec_b64 s[16:17], vcc
	s_cbranch_execnz .LBB0_14
	s_branch .LBB0_15

	.amdhsa_kernel _Z9nerf_prepPKfS0_S0_S0_S0_S0_S0_S0_S0_S0_S0_PtPf
		.amdhsa_group_segment_fixed_size 0
		.amdhsa_private_segment_fixed_size 0
		.amdhsa_kernarg_size 104
		.amdhsa_user_sgpr_count 2
		.amdhsa_user_sgpr_dispatch_ptr 0
		.amdhsa_user_sgpr_queue_ptr 0
		.amdhsa_user_sgpr_kernarg_segment_ptr 1
		.amdhsa_user_sgpr_dispatch_id 0
		.amdhsa_user_sgpr_kernarg_preload_length 0
		.amdhsa_user_sgpr_kernarg_preload_offset 0
		.amdhsa_user_sgpr_private_segment_size 0
		.amdhsa_uses_dynamic_stack 0
		.amdhsa_enable_private_segment 0
		.amdhsa_system_sgpr_workgroup_id_x 1
		.amdhsa_system_sgpr_workgroup_id_y 0
		.amdhsa_system_sgpr_workgroup_id_z 0
		.amdhsa_system_sgpr_workgroup_info 0
		.amdhsa_system_vgpr_workitem_id 0
		.amdhsa_next_free_vgpr 62
		.amdhsa_next_free_sgpr 40
		.amdhsa_accum_offset 64
		.amdhsa_reserve_vcc 1
		.amdhsa_float_round_mode_32 0
		.amdhsa_float_round_mode_16_64 0
		.amdhsa_float_denorm_mode_32 3
		.amdhsa_float_denorm_mode_16_64 3
		.amdhsa_dx10_clamp 1
		.amdhsa_ieee_mode 1
		.amdhsa_fp16_overflow 0
		.amdhsa_tg_split 0
		.amdhsa_exception_fp_ieee_invalid_op 0
		.amdhsa_exception_fp_denorm_src 0
		.amdhsa_exception_fp_ieee_div_zero 0
		.amdhsa_exception_fp_ieee_overflow 0
		.amdhsa_exception_fp_ieee_underflow 0
		.amdhsa_exception_fp_ieee_inexact 0
		.amdhsa_exception_int_div_zero 0
	.end_amdhsa_kernel

amdhsa.kernels:
  - .agpr_count:     0
    .args:
      - .actual_access:  read_only
        .address_space:  global
        .offset:         0
        .size:           8
        .value_kind:     global_buffer
      - .actual_access:  read_only
        .address_space:  global
        .offset:         8
        .size:           8
        .value_kind:     global_buffer
      - .actual_access:  read_only
        .address_space:  global
        .offset:         16
        .size:           8
        .value_kind:     global_buffer
      - .actual_access:  read_only
        .address_space:  global
        .offset:         24
        .size:           8
        .value_kind:     global_buffer
      - .actual_access:  read_only
        .address_space:  global
        .offset:         32
        .size:           8
        .value_kind:     global_buffer
      - .actual_access:  read_only
        .address_space:  global
        .offset:         40
        .size:           8
        .value_kind:     global_buffer
      - .actual_access:  read_only
        .address_space:  global
        .offset:         48
        .size:           8
        .value_kind:     global_buffer
      - .actual_access:  read_only
        .address_space:  global
        .offset:         56
        .size:           8
        .value_kind:     global_buffer
      - .actual_access:  read_only
        .address_space:  global
        .offset:         64
        .size:           8
        .value_kind:     global_buffer
      - .actual_access:  read_only
        .address_space:  global
        .offset:         72
        .size:           8
        .value_kind:     global_buffer
      - .actual_access:  read_only
        .address_space:  global
        .offset:         80
        .size:           8
        .value_kind:     global_buffer
      - .actual_access:  write_only
        .address_space:  global
        .offset:         88
        .size:           8
        .value_kind:     global_buffer
      - .actual_access:  write_only
        .address_space:  global
        .offset:         96
        .size:           8
        .value_kind:     global_buffer
    .group_segment_fixed_size: 0
    .kernarg_segment_align: 8
    .kernarg_segment_size: 104
    .language:       OpenCL C
    .language_version:
      - 2
      - 0
    .max_flat_workgroup_size: 256
    .name:           _Z9nerf_prepPKfS0_S0_S0_S0_S0_S0_S0_S0_S0_S0_PtPf
    .private_segment_fixed_size: 0
    .sgpr_count:     46
    .sgpr_spill_count: 0
    .symbol:         _Z9nerf_prepPKfS0_S0_S0_S0_S0_S0_S0_S0_S0_S0_PtPf.kd
    .uniform_work_group_size: 1
    .uses_dynamic_stack: false
    .vgpr_count:     62
    .vgpr_spill_count: 0
    .wavefront_size: 64
  - .agpr_count:     0
    .args:
      - .actual_access:  read_only
        .address_space:  global
        .offset:         0
        .size:           8
        .value_kind:     global_buffer
      - .actual_access:  read_only
        .address_space:  global
        .offset:         8
        .size:           8
        .value_kind:     global_buffer
      - .actual_access:  read_only
        .address_space:  global
        .offset:         16
        .size:           8
        .value_kind:     global_buffer
      - .actual_access:  read_only
        .address_space:  global
        .offset:         24
        .size:           8
        .value_kind:     global_buffer
      - .actual_access:  read_only
        .address_space:  global
        .offset:         32
        .size:           8
        .value_kind:     global_buffer
      - .actual_access:  read_only
        .address_space:  global
        .offset:         40
        .size:           8
        .value_kind:     global_buffer
      - .actual_access:  read_only
        .address_space:  global
        .offset:         48
        .size:           8
        .value_kind:     global_buffer
      - .actual_access:  write_only
        .address_space:  global
        .offset:         56
        .size:           8
        .value_kind:     global_buffer
    .group_segment_fixed_size: 147456
    .kernarg_segment_align: 8
    .kernarg_segment_size: 64
    .language:       OpenCL C
    .language_version:
      - 2
      - 0
    .max_flat_workgroup_size: 512
    .name:           _Z9nerf_mainPKfS0_S0_PKiS2_PKcS0_Pf
    .private_segment_fixed_size: 0
    .sgpr_count:     55
    .sgpr_spill_count: 0
    .symbol:         _Z9nerf_mainPKfS0_S0_PKiS2_PKcS0_Pf.kd
    .uniform_work_group_size: 1
    .uses_dynamic_stack: false
    .vgpr_count:     256
    .vgpr_spill_count: 0
    .wavefront_size: 64
